# E34: E33 + MoE-down epilogue prefetches all 8 row-group slot indices and gates up front (2 round trips per unit instead of 16)
# speedup vs baseline: 1.0144x; 1.0144x over previous
.LBB0_1713:
	s_lshl_b32 s7, s30, 2
	s_add_i32 s7, s7, 0
	s_add_i32 s7, s7, 0x22700
	v_mov_b32_e32 v142, s7
	ds_read_b32 v142, v142
	s_lshl_b32 s7, s52, 2
	s_add_i32 s7, s7, 0
	s_add_i32 s7, s7, 0x22c00
	s_waitcnt lgkmcnt(0)
	v_readfirstlane_b32 s25, v142
	v_mov_b32_e32 v142, s7
	ds_read_b32 v142, v142
	v_add_u32_e32 v147, s25, v131
	s_waitcnt lgkmcnt(0)
	v_readfirstlane_b32 s7, v142
	s_nop 1
	v_cmp_gt_i32_e32 vcc, s7, v147
	v_lshl_or_b32 v142, s6, 8, v145
	s_add_i32 s34, s52, s50
	s_ashr_i32 s35, s34, 31
	s_lshl_b64 s[34:35], s[34:35], 12
	s_add_u32 s34, s44, s34
	v_ashrrev_i32_e32 v143, 31, v142
	s_addc_u32 s35, s16, s35
	v_lshl_add_u64 v[162:163], v[142:143], 2, s[34:35]
	global_load_dwordx4 v[164:167], v[162:163], off
	global_load_dwordx4 v[168:171], v[162:163], off offset:16
	global_load_dwordx4 v[172:175], v[162:163], off offset:512
	global_load_dwordx4 v[176:179], v[162:163], off offset:528
	v_cmp_gt_i32_e32 vcc, s7, v147
	s_and_saveexec_b64 s[30:31], vcc
	v_lshl_add_u32 v196, s52, 14, v147
	v_ashrrev_i32_e32 v197, 31, v196
	v_lshl_add_u64 v[196:197], v[196:197], 2, s[12:13]
	global_load_dword v180, v[196:197], off
	s_or_b64 exec, exec, s[30:31]
	v_add_u32_e32 v198, 16, v147
	v_cmp_gt_i32_e32 vcc, s7, v198
	s_and_saveexec_b64 s[30:31], vcc
	v_lshl_add_u32 v196, s52, 14, v198
	v_ashrrev_i32_e32 v197, 31, v196
	v_lshl_add_u64 v[196:197], v[196:197], 2, s[12:13]
	global_load_dword v181, v[196:197], off
	s_or_b64 exec, exec, s[30:31]
	v_add_u32_e32 v198, 32, v147
	v_cmp_gt_i32_e32 vcc, s7, v198
	s_and_saveexec_b64 s[30:31], vcc
	v_lshl_add_u32 v196, s52, 14, v198
	v_ashrrev_i32_e32 v197, 31, v196
	v_lshl_add_u64 v[196:197], v[196:197], 2, s[12:13]
	global_load_dword v182, v[196:197], off
	s_or_b64 exec, exec, s[30:31]
	v_add_u32_e32 v198, 48, v147
	v_cmp_gt_i32_e32 vcc, s7, v198
	s_and_saveexec_b64 s[30:31], vcc
	v_lshl_add_u32 v196, s52, 14, v198
	v_ashrrev_i32_e32 v197, 31, v196
	v_lshl_add_u64 v[196:197], v[196:197], 2, s[12:13]
	global_load_dword v183, v[196:197], off
	s_or_b64 exec, exec, s[30:31]
	v_add_u32_e32 v198, 128, v147
	v_cmp_gt_i32_e32 vcc, s7, v198
	s_and_saveexec_b64 s[30:31], vcc
	v_lshl_add_u32 v196, s52, 14, v198
	v_ashrrev_i32_e32 v197, 31, v196
	v_lshl_add_u64 v[196:197], v[196:197], 2, s[12:13]
	global_load_dword v184, v[196:197], off
	s_or_b64 exec, exec, s[30:31]
	v_add_u32_e32 v198, 144, v147
	v_cmp_gt_i32_e32 vcc, s7, v198
	s_and_saveexec_b64 s[30:31], vcc
	v_lshl_add_u32 v196, s52, 14, v198
	v_ashrrev_i32_e32 v197, 31, v196
	v_lshl_add_u64 v[196:197], v[196:197], 2, s[12:13]
	global_load_dword v185, v[196:197], off
	s_or_b64 exec, exec, s[30:31]
	v_add_u32_e32 v198, 160, v147
	v_cmp_gt_i32_e32 vcc, s7, v198
	s_and_saveexec_b64 s[30:31], vcc
	v_lshl_add_u32 v196, s52, 14, v198
	v_ashrrev_i32_e32 v197, 31, v196
	v_lshl_add_u64 v[196:197], v[196:197], 2, s[12:13]
	global_load_dword v186, v[196:197], off
	s_or_b64 exec, exec, s[30:31]
	v_add_u32_e32 v198, 176, v147
	v_cmp_gt_i32_e32 vcc, s7, v198
	s_and_saveexec_b64 s[30:31], vcc
	v_lshl_add_u32 v196, s52, 14, v198
	v_ashrrev_i32_e32 v197, 31, v196
	v_lshl_add_u64 v[196:197], v[196:197], 2, s[12:13]
	global_load_dword v187, v[196:197], off
	s_or_b64 exec, exec, s[30:31]
	s_waitcnt vmcnt(0)
	v_cmp_gt_i32_e32 vcc, s7, v147
	s_and_saveexec_b64 s[30:31], vcc
	v_mov_b32_e32 v196, v180
	v_ashrrev_i32_e32 v197, 31, v196
	v_lshl_add_u64 v[196:197], v[196:197], 2, s[14:15]
	global_load_dword v188, v[196:197], off
	s_or_b64 exec, exec, s[30:31]
	v_add_u32_e32 v198, 16, v147
	v_cmp_gt_i32_e32 vcc, s7, v198
	s_and_saveexec_b64 s[30:31], vcc
	v_mov_b32_e32 v196, v181
	v_ashrrev_i32_e32 v197, 31, v196
	v_lshl_add_u64 v[196:197], v[196:197], 2, s[14:15]
	global_load_dword v189, v[196:197], off
	s_or_b64 exec, exec, s[30:31]
	v_add_u32_e32 v198, 32, v147
	v_cmp_gt_i32_e32 vcc, s7, v198
	s_and_saveexec_b64 s[30:31], vcc
	v_mov_b32_e32 v196, v182
	v_ashrrev_i32_e32 v197, 31, v196
	v_lshl_add_u64 v[196:197], v[196:197], 2, s[14:15]
	global_load_dword v190, v[196:197], off
	s_or_b64 exec, exec, s[30:31]
	v_add_u32_e32 v198, 48, v147
	v_cmp_gt_i32_e32 vcc, s7, v198
	s_and_saveexec_b64 s[30:31], vcc
	v_mov_b32_e32 v196, v183
	v_ashrrev_i32_e32 v197, 31, v196
	v_lshl_add_u64 v[196:197], v[196:197], 2, s[14:15]
	global_load_dword v191, v[196:197], off
	s_or_b64 exec, exec, s[30:31]
	v_add_u32_e32 v198, 128, v147
	v_cmp_gt_i32_e32 vcc, s7, v198
	s_and_saveexec_b64 s[30:31], vcc
	v_mov_b32_e32 v196, v184
	v_ashrrev_i32_e32 v197, 31, v196
	v_lshl_add_u64 v[196:197], v[196:197], 2, s[14:15]
	global_load_dword v192, v[196:197], off
	s_or_b64 exec, exec, s[30:31]
	v_add_u32_e32 v198, 144, v147
	v_cmp_gt_i32_e32 vcc, s7, v198
	s_and_saveexec_b64 s[30:31], vcc
	v_mov_b32_e32 v196, v185
	v_ashrrev_i32_e32 v197, 31, v196
	v_lshl_add_u64 v[196:197], v[196:197], 2, s[14:15]
	global_load_dword v193, v[196:197], off
	s_or_b64 exec, exec, s[30:31]
	v_add_u32_e32 v198, 160, v147
	v_cmp_gt_i32_e32 vcc, s7, v198
	s_and_saveexec_b64 s[30:31], vcc
	v_mov_b32_e32 v196, v186
	v_ashrrev_i32_e32 v197, 31, v196
	v_lshl_add_u64 v[196:197], v[196:197], 2, s[14:15]
	global_load_dword v194, v[196:197], off
	s_or_b64 exec, exec, s[30:31]
	v_add_u32_e32 v198, 176, v147
	v_cmp_gt_i32_e32 vcc, s7, v198
	s_and_saveexec_b64 s[30:31], vcc
	v_mov_b32_e32 v196, v187
	v_ashrrev_i32_e32 v197, 31, v196
	v_lshl_add_u64 v[196:197], v[196:197], 2, s[14:15]
	global_load_dword v195, v[196:197], off
	s_or_b64 exec, exec, s[30:31]
	s_waitcnt vmcnt(0)
	v_cmp_gt_i32_e32 vcc, s7, v147
	s_and_saveexec_b64 s[30:31], vcc
	s_cbranch_execz .LBB0_1715
	v_lshl_add_u32 v148, s52, 14, v147
	v_ashrrev_i32_e32 v149, 31, v148
	v_lshl_add_u64 v[148:149], v[148:149], 2, s[12:13]
	v_mov_b32_e32 v156, v180
	s_add_i32 s34, s52, s50
	s_ashr_i32 s35, s34, 31
	s_lshl_b64 s[34:35], s[34:35], 12
	s_add_u32 s34, s44, s34
	v_ashrrev_i32_e32 v143, 31, v142
	s_addc_u32 s35, s16, s35
	v_lshl_add_u64 v[158:159], v[142:143], 2, s[34:35]
	v_ashrrev_i32_e32 v157, 31, v156
	v_lshl_add_u64 v[160:161], v[156:157], 2, s[14:15]
	v_mov_b32_e32 v160, v188
	v_lshlrev_b64 v[156:157], 11, v[156:157]
	v_lshl_add_u64 v[156:157], s[10:11], 0, v[156:157]
	v_pk_add_f32 v[128:129], v[128:129], v[166:167]
	v_pk_add_f32 v[124:125], v[124:125], v[170:171]
	v_pk_add_f32 v[122:123], v[122:123], v[168:169]
	v_pk_add_f32 v[126:127], v[126:127], v[164:165]
	v_lshl_add_u64 v[148:149], v[142:143], 1, v[156:157]
	v_pk_mul_f32 v[150:151], v[160:161], v[124:125] op_sel_hi:[0,1]
	v_pk_mul_f32 v[124:125], v[160:161], v[122:123] op_sel_hi:[0,1]
	v_pk_mul_f32 v[128:129], v[160:161], v[128:129] op_sel_hi:[0,1]
	v_pk_mul_f32 v[126:127], v[160:161], v[126:127] op_sel_hi:[0,1]
	v_cvt_pk_bf16_f32 v122, v126, v127
	v_cvt_pk_bf16_f32 v123, v128, v129
	v_cvt_pk_bf16_f32 v124, v124, v125
	v_cvt_pk_bf16_f32 v125, v150, v151
	global_store_dwordx4 v[148:149], v[122:125], off
	v_pk_add_f32 v[120:121], v[120:121], v[174:175]
	v_pk_add_f32 v[116:117], v[116:117], v[178:179]
	v_pk_add_f32 v[114:115], v[114:115], v[176:177]
	v_pk_add_f32 v[118:119], v[118:119], v[172:173]
	v_pk_mul_f32 v[122:123], v[160:161], v[116:117] op_sel_hi:[0,1]
	v_pk_mul_f32 v[116:117], v[160:161], v[114:115] op_sel_hi:[0,1]
	v_pk_mul_f32 v[120:121], v[160:161], v[120:121] op_sel_hi:[0,1]
	v_pk_mul_f32 v[118:119], v[160:161], v[118:119] op_sel_hi:[0,1]
	v_cvt_pk_bf16_f32 v114, v118, v119
	v_cvt_pk_bf16_f32 v115, v120, v121
	v_cvt_pk_bf16_f32 v116, v116, v117
	v_cvt_pk_bf16_f32 v117, v122, v123
	global_store_dwordx4 v[148:149], v[114:117], off offset:256
.LBB0_1715:
	s_or_b64 exec, exec, s[30:31]
	s_nop 0
	v_add_u32_e32 v114, 16, v147
	v_cmp_gt_i32_e32 vcc, s7, v114
	s_and_saveexec_b64 s[30:31], vcc
	s_cbranch_execz .LBB0_1717
	v_lshl_add_u32 v114, s52, 14, v114
	v_ashrrev_i32_e32 v115, 31, v114
	v_lshl_add_u64 v[114:115], v[114:115], 2, s[12:13]
	v_mov_b32_e32 v122, v181
	s_add_i32 s34, s52, s50
	s_ashr_i32 s35, s34, 31
	s_lshl_b64 s[34:35], s[34:35], 12
	s_add_u32 s34, s44, s34
	v_ashrrev_i32_e32 v143, 31, v142
	s_addc_u32 s35, s16, s35
	v_lshl_add_u64 v[124:125], v[142:143], 2, s[34:35]
	v_ashrrev_i32_e32 v123, 31, v122
	v_lshl_add_u64 v[126:127], v[122:123], 2, s[14:15]
	v_mov_b32_e32 v126, v189
	v_lshlrev_b64 v[122:123], 11, v[122:123]
	v_lshl_add_u64 v[122:123], s[10:11], 0, v[122:123]
	v_pk_add_f32 v[112:113], v[112:113], v[166:167]
	v_pk_add_f32 v[108:109], v[108:109], v[170:171]
	v_pk_add_f32 v[106:107], v[106:107], v[168:169]
	v_pk_add_f32 v[110:111], v[110:111], v[164:165]
	v_lshl_add_u64 v[114:115], v[142:143], 1, v[122:123]
	v_pk_mul_f32 v[116:117], v[126:127], v[108:109] op_sel_hi:[0,1]
	v_pk_mul_f32 v[108:109], v[126:127], v[106:107] op_sel_hi:[0,1]
	v_pk_mul_f32 v[112:113], v[126:127], v[112:113] op_sel_hi:[0,1]
	v_pk_mul_f32 v[110:111], v[126:127], v[110:111] op_sel_hi:[0,1]
	v_cvt_pk_bf16_f32 v106, v110, v111
	v_cvt_pk_bf16_f32 v107, v112, v113
	v_cvt_pk_bf16_f32 v108, v108, v109
	v_cvt_pk_bf16_f32 v109, v116, v117
	global_store_dwordx4 v[114:115], v[106:109], off
	v_pk_add_f32 v[104:105], v[104:105], v[174:175]
	v_pk_add_f32 v[98:99], v[98:99], v[178:179]
	v_pk_add_f32 v[96:97], v[96:97], v[176:177]
	v_pk_add_f32 v[102:103], v[102:103], v[172:173]
	v_pk_mul_f32 v[106:107], v[126:127], v[98:99] op_sel_hi:[0,1]
	v_pk_mul_f32 v[98:99], v[126:127], v[96:97] op_sel_hi:[0,1]
	v_pk_mul_f32 v[104:105], v[126:127], v[104:105] op_sel_hi:[0,1]
	v_pk_mul_f32 v[102:103], v[126:127], v[102:103] op_sel_hi:[0,1]
	v_cvt_pk_bf16_f32 v96, v102, v103
	v_cvt_pk_bf16_f32 v97, v104, v105
	v_cvt_pk_bf16_f32 v98, v98, v99
	v_cvt_pk_bf16_f32 v99, v106, v107
	global_store_dwordx4 v[114:115], v[96:99], off offset:256
.LBB0_1717:
	s_or_b64 exec, exec, s[30:31]
	s_nop 0
	v_add_u32_e32 v96, 32, v147
	v_cmp_gt_i32_e32 vcc, s7, v96
	s_and_saveexec_b64 s[30:31], vcc
	s_cbranch_execz .LBB0_1719
	v_lshl_add_u32 v96, s52, 14, v96
	v_ashrrev_i32_e32 v97, 31, v96
	v_lshl_add_u64 v[96:97], v[96:97], 2, s[12:13]
	v_mov_b32_e32 v106, v182
	s_add_i32 s34, s52, s50
	s_ashr_i32 s35, s34, 31
	s_lshl_b64 s[34:35], s[34:35], 12
	s_add_u32 s34, s44, s34
	v_ashrrev_i32_e32 v143, 31, v142
	s_addc_u32 s35, s16, s35
	v_lshl_add_u64 v[108:109], v[142:143], 2, s[34:35]
	v_ashrrev_i32_e32 v107, 31, v106
	v_lshl_add_u64 v[110:111], v[106:107], 2, s[14:15]
	v_mov_b32_e32 v110, v190
	v_lshlrev_b64 v[106:107], 11, v[106:107]
	v_lshl_add_u64 v[106:107], s[10:11], 0, v[106:107]
	v_pk_add_f32 v[94:95], v[94:95], v[166:167]
	v_pk_add_f32 v[90:91], v[90:91], v[170:171]
	v_pk_add_f32 v[88:89], v[88:89], v[168:169]
	v_pk_add_f32 v[92:93], v[92:93], v[164:165]
	v_lshl_add_u64 v[96:97], v[142:143], 1, v[106:107]
	v_pk_mul_f32 v[98:99], v[110:111], v[90:91] op_sel_hi:[0,1]
	v_pk_mul_f32 v[90:91], v[110:111], v[88:89] op_sel_hi:[0,1]
	v_pk_mul_f32 v[94:95], v[110:111], v[94:95] op_sel_hi:[0,1]
	v_pk_mul_f32 v[92:93], v[110:111], v[92:93] op_sel_hi:[0,1]
	v_cvt_pk_bf16_f32 v88, v92, v93
	v_cvt_pk_bf16_f32 v89, v94, v95
	v_cvt_pk_bf16_f32 v90, v90, v91
	v_cvt_pk_bf16_f32 v91, v98, v99
	global_store_dwordx4 v[96:97], v[88:91], off
	v_pk_add_f32 v[86:87], v[86:87], v[174:175]
	v_pk_add_f32 v[82:83], v[82:83], v[178:179]
	v_pk_add_f32 v[80:81], v[80:81], v[176:177]
	v_pk_add_f32 v[84:85], v[84:85], v[172:173]
	v_pk_mul_f32 v[88:89], v[110:111], v[82:83] op_sel_hi:[0,1]
	v_pk_mul_f32 v[82:83], v[110:111], v[80:81] op_sel_hi:[0,1]
	v_pk_mul_f32 v[86:87], v[110:111], v[86:87] op_sel_hi:[0,1]
	v_pk_mul_f32 v[84:85], v[110:111], v[84:85] op_sel_hi:[0,1]
	v_cvt_pk_bf16_f32 v80, v84, v85
	v_cvt_pk_bf16_f32 v81, v86, v87
	v_cvt_pk_bf16_f32 v82, v82, v83
	v_cvt_pk_bf16_f32 v83, v88, v89
	global_store_dwordx4 v[96:97], v[80:83], off offset:256
.LBB0_1719:
	s_or_b64 exec, exec, s[30:31]
	s_nop 0
	v_add_u32_e32 v80, 48, v147
	v_cmp_gt_i32_e32 vcc, s7, v80
	s_and_saveexec_b64 s[30:31], vcc
	s_cbranch_execz .LBB0_1721
	v_lshl_add_u32 v80, s52, 14, v80
	v_ashrrev_i32_e32 v81, 31, v80
	v_lshl_add_u64 v[80:81], v[80:81], 2, s[12:13]
	v_mov_b32_e32 v88, v183
	s_add_i32 s34, s52, s50
	s_ashr_i32 s35, s34, 31
	s_lshl_b64 s[34:35], s[34:35], 12
	s_add_u32 s34, s44, s34
	v_ashrrev_i32_e32 v143, 31, v142
	s_addc_u32 s35, s16, s35
	v_lshl_add_u64 v[90:91], v[142:143], 2, s[34:35]
	v_ashrrev_i32_e32 v89, 31, v88
	v_lshl_add_u64 v[92:93], v[88:89], 2, s[14:15]
	v_mov_b32_e32 v92, v191
	v_lshlrev_b64 v[88:89], 11, v[88:89]
	v_lshl_add_u64 v[88:89], s[10:11], 0, v[88:89]
	v_pk_add_f32 v[78:79], v[78:79], v[166:167]
	v_pk_add_f32 v[74:75], v[74:75], v[170:171]
	v_pk_add_f32 v[72:73], v[72:73], v[168:169]
	v_pk_add_f32 v[76:77], v[76:77], v[164:165]
	v_lshl_add_u64 v[80:81], v[142:143], 1, v[88:89]
	v_pk_mul_f32 v[82:83], v[92:93], v[74:75] op_sel_hi:[0,1]
	v_pk_mul_f32 v[74:75], v[92:93], v[72:73] op_sel_hi:[0,1]
	v_pk_mul_f32 v[78:79], v[92:93], v[78:79] op_sel_hi:[0,1]
	v_pk_mul_f32 v[76:77], v[92:93], v[76:77] op_sel_hi:[0,1]
	v_cvt_pk_bf16_f32 v72, v76, v77
	v_cvt_pk_bf16_f32 v73, v78, v79
	v_cvt_pk_bf16_f32 v74, v74, v75
	v_cvt_pk_bf16_f32 v75, v82, v83
	global_store_dwordx4 v[80:81], v[72:75], off
	v_pk_add_f32 v[70:71], v[70:71], v[174:175]
	v_pk_add_f32 v[66:67], v[66:67], v[178:179]
	v_pk_add_f32 v[64:65], v[64:65], v[176:177]
	v_pk_add_f32 v[68:69], v[68:69], v[172:173]
	v_pk_mul_f32 v[72:73], v[92:93], v[66:67] op_sel_hi:[0,1]
	v_pk_mul_f32 v[66:67], v[92:93], v[64:65] op_sel_hi:[0,1]
	v_pk_mul_f32 v[70:71], v[92:93], v[70:71] op_sel_hi:[0,1]
	v_pk_mul_f32 v[68:69], v[92:93], v[68:69] op_sel_hi:[0,1]
	v_cvt_pk_bf16_f32 v64, v68, v69
	v_cvt_pk_bf16_f32 v65, v70, v71
	v_cvt_pk_bf16_f32 v66, v66, v67
	v_cvt_pk_bf16_f32 v67, v72, v73
	global_store_dwordx4 v[80:81], v[64:67], off offset:256
.LBB0_1721:
	s_or_b64 exec, exec, s[30:31]
	s_nop 0
	v_add_u32_e32 v64, 0x80, v147
	v_cmp_gt_i32_e32 vcc, s7, v64
	s_and_saveexec_b64 s[30:31], vcc
	s_cbranch_execz .LBB0_1723
	v_lshl_add_u32 v64, s52, 14, v64
	v_ashrrev_i32_e32 v65, 31, v64
	v_lshl_add_u64 v[64:65], v[64:65], 2, s[12:13]
	v_mov_b32_e32 v72, v184
	s_add_i32 s34, s52, s50
	s_ashr_i32 s35, s34, 31
	s_lshl_b64 s[34:35], s[34:35], 12
	s_add_u32 s34, s44, s34
	v_ashrrev_i32_e32 v143, 31, v142
	s_addc_u32 s35, s16, s35
	v_lshl_add_u64 v[74:75], v[142:143], 2, s[34:35]
	v_ashrrev_i32_e32 v73, 31, v72
	v_lshl_add_u64 v[76:77], v[72:73], 2, s[14:15]
	v_mov_b32_e32 v76, v192
	v_lshlrev_b64 v[72:73], 11, v[72:73]
	v_lshl_add_u64 v[72:73], s[10:11], 0, v[72:73]
	v_pk_add_f32 v[62:63], v[62:63], v[166:167]
	v_pk_add_f32 v[58:59], v[58:59], v[170:171]
	v_pk_add_f32 v[56:57], v[56:57], v[168:169]
	v_pk_add_f32 v[60:61], v[60:61], v[164:165]
	v_lshl_add_u64 v[64:65], v[142:143], 1, v[72:73]
	v_pk_mul_f32 v[66:67], v[76:77], v[58:59] op_sel_hi:[0,1]
	v_pk_mul_f32 v[58:59], v[76:77], v[56:57] op_sel_hi:[0,1]
	v_pk_mul_f32 v[62:63], v[76:77], v[62:63] op_sel_hi:[0,1]
	v_pk_mul_f32 v[60:61], v[76:77], v[60:61] op_sel_hi:[0,1]
	v_cvt_pk_bf16_f32 v56, v60, v61
	v_cvt_pk_bf16_f32 v57, v62, v63
	v_cvt_pk_bf16_f32 v58, v58, v59
	v_cvt_pk_bf16_f32 v59, v66, v67
	global_store_dwordx4 v[64:65], v[56:59], off
	v_pk_add_f32 v[54:55], v[54:55], v[174:175]
	v_pk_add_f32 v[50:51], v[50:51], v[178:179]
	v_pk_add_f32 v[48:49], v[48:49], v[176:177]
	v_pk_add_f32 v[52:53], v[52:53], v[172:173]
	v_pk_mul_f32 v[56:57], v[76:77], v[50:51] op_sel_hi:[0,1]
	v_pk_mul_f32 v[50:51], v[76:77], v[48:49] op_sel_hi:[0,1]
	v_pk_mul_f32 v[54:55], v[76:77], v[54:55] op_sel_hi:[0,1]
	v_pk_mul_f32 v[52:53], v[76:77], v[52:53] op_sel_hi:[0,1]
	v_cvt_pk_bf16_f32 v48, v52, v53
	v_cvt_pk_bf16_f32 v49, v54, v55
	v_cvt_pk_bf16_f32 v50, v50, v51
	v_cvt_pk_bf16_f32 v51, v56, v57
	global_store_dwordx4 v[64:65], v[48:51], off offset:256
.LBB0_1723:
	s_or_b64 exec, exec, s[30:31]
	s_nop 0
	v_add_u32_e32 v48, 0x90, v147
	v_cmp_gt_i32_e32 vcc, s7, v48
	s_and_saveexec_b64 s[30:31], vcc
	s_cbranch_execz .LBB0_1725
	v_lshl_add_u32 v48, s52, 14, v48
	v_ashrrev_i32_e32 v49, 31, v48
	v_lshl_add_u64 v[48:49], v[48:49], 2, s[12:13]
	v_mov_b32_e32 v56, v185
	s_add_i32 s34, s52, s50
	s_ashr_i32 s35, s34, 31
	s_lshl_b64 s[34:35], s[34:35], 12
	s_add_u32 s34, s44, s34
	v_ashrrev_i32_e32 v143, 31, v142
	s_addc_u32 s35, s16, s35
	v_lshl_add_u64 v[58:59], v[142:143], 2, s[34:35]
	v_ashrrev_i32_e32 v57, 31, v56
	v_lshl_add_u64 v[60:61], v[56:57], 2, s[14:15]
	v_mov_b32_e32 v60, v193
	v_lshlrev_b64 v[56:57], 11, v[56:57]
	v_lshl_add_u64 v[56:57], s[10:11], 0, v[56:57]
	v_pk_add_f32 v[46:47], v[46:47], v[166:167]
	v_pk_add_f32 v[42:43], v[42:43], v[170:171]
	v_pk_add_f32 v[40:41], v[40:41], v[168:169]
	v_pk_add_f32 v[44:45], v[44:45], v[164:165]
	v_lshl_add_u64 v[48:49], v[142:143], 1, v[56:57]
	v_pk_mul_f32 v[50:51], v[60:61], v[42:43] op_sel_hi:[0,1]
	v_pk_mul_f32 v[42:43], v[60:61], v[40:41] op_sel_hi:[0,1]
	v_pk_mul_f32 v[46:47], v[60:61], v[46:47] op_sel_hi:[0,1]
	v_pk_mul_f32 v[44:45], v[60:61], v[44:45] op_sel_hi:[0,1]
	v_cvt_pk_bf16_f32 v40, v44, v45
	v_cvt_pk_bf16_f32 v41, v46, v47
	v_cvt_pk_bf16_f32 v42, v42, v43
	v_cvt_pk_bf16_f32 v43, v50, v51
	global_store_dwordx4 v[48:49], v[40:43], off
	v_pk_add_f32 v[38:39], v[38:39], v[174:175]
	v_pk_add_f32 v[34:35], v[34:35], v[178:179]
	v_pk_add_f32 v[32:33], v[32:33], v[176:177]
	v_pk_add_f32 v[36:37], v[36:37], v[172:173]
	v_pk_mul_f32 v[40:41], v[60:61], v[34:35] op_sel_hi:[0,1]
	v_pk_mul_f32 v[34:35], v[60:61], v[32:33] op_sel_hi:[0,1]
	v_pk_mul_f32 v[38:39], v[60:61], v[38:39] op_sel_hi:[0,1]
	v_pk_mul_f32 v[36:37], v[60:61], v[36:37] op_sel_hi:[0,1]
	v_cvt_pk_bf16_f32 v32, v36, v37
	v_cvt_pk_bf16_f32 v33, v38, v39
	v_cvt_pk_bf16_f32 v34, v34, v35
	v_cvt_pk_bf16_f32 v35, v40, v41
	global_store_dwordx4 v[48:49], v[32:35], off offset:256
.LBB0_1725:
	s_or_b64 exec, exec, s[30:31]
	s_nop 0
	v_add_u32_e32 v32, 0xa0, v147
	v_cmp_gt_i32_e32 vcc, s7, v32
	s_and_saveexec_b64 s[30:31], vcc
	s_cbranch_execz .LBB0_1727
	v_lshl_add_u32 v32, s52, 14, v32
	v_ashrrev_i32_e32 v33, 31, v32
	v_lshl_add_u64 v[32:33], v[32:33], 2, s[12:13]
	v_mov_b32_e32 v40, v186
	s_add_i32 s34, s52, s50
	s_ashr_i32 s35, s34, 31
	s_lshl_b64 s[34:35], s[34:35], 12
	s_add_u32 s34, s44, s34
	v_ashrrev_i32_e32 v143, 31, v142
	s_addc_u32 s35, s16, s35
	v_lshl_add_u64 v[42:43], v[142:143], 2, s[34:35]
	v_ashrrev_i32_e32 v41, 31, v40
	v_lshl_add_u64 v[44:45], v[40:41], 2, s[14:15]
	v_mov_b32_e32 v44, v194
	v_lshlrev_b64 v[40:41], 11, v[40:41]
	v_lshl_add_u64 v[40:41], s[10:11], 0, v[40:41]
	v_pk_add_f32 v[30:31], v[30:31], v[166:167]
	v_pk_add_f32 v[26:27], v[26:27], v[170:171]
	v_pk_add_f32 v[24:25], v[24:25], v[168:169]
	v_pk_add_f32 v[28:29], v[28:29], v[164:165]
	v_lshl_add_u64 v[32:33], v[142:143], 1, v[40:41]
	v_pk_mul_f32 v[34:35], v[44:45], v[26:27] op_sel_hi:[0,1]
	v_pk_mul_f32 v[26:27], v[44:45], v[24:25] op_sel_hi:[0,1]
	v_pk_mul_f32 v[30:31], v[44:45], v[30:31] op_sel_hi:[0,1]
	v_pk_mul_f32 v[28:29], v[44:45], v[28:29] op_sel_hi:[0,1]
	v_cvt_pk_bf16_f32 v24, v28, v29
	v_cvt_pk_bf16_f32 v25, v30, v31
	v_cvt_pk_bf16_f32 v26, v26, v27
	v_cvt_pk_bf16_f32 v27, v34, v35
	global_store_dwordx4 v[32:33], v[24:27], off
	v_pk_add_f32 v[22:23], v[22:23], v[174:175]
	v_pk_add_f32 v[18:19], v[18:19], v[178:179]
	v_pk_add_f32 v[16:17], v[16:17], v[176:177]
	v_pk_add_f32 v[20:21], v[20:21], v[172:173]
	v_pk_mul_f32 v[24:25], v[44:45], v[18:19] op_sel_hi:[0,1]
	v_pk_mul_f32 v[18:19], v[44:45], v[16:17] op_sel_hi:[0,1]
	v_pk_mul_f32 v[22:23], v[44:45], v[22:23] op_sel_hi:[0,1]
	v_pk_mul_f32 v[20:21], v[44:45], v[20:21] op_sel_hi:[0,1]
	v_cvt_pk_bf16_f32 v16, v20, v21
	v_cvt_pk_bf16_f32 v17, v22, v23
	v_cvt_pk_bf16_f32 v18, v18, v19
	v_cvt_pk_bf16_f32 v19, v24, v25
	global_store_dwordx4 v[32:33], v[16:19], off offset:256
.LBB0_1727:
	s_or_b64 exec, exec, s[30:31]
	s_nop 0
	v_add_u32_e32 v16, 0xb0, v147
	v_cmp_gt_i32_e32 vcc, s7, v16
	s_and_saveexec_b64 s[30:31], vcc
	s_cbranch_execz .LBB0_1729
	v_lshl_add_u32 v16, s52, 14, v16
	v_ashrrev_i32_e32 v17, 31, v16
	v_lshl_add_u64 v[16:17], v[16:17], 2, s[12:13]
	v_mov_b32_e32 v24, v187
	s_add_i32 s34, s52, s50
	s_ashr_i32 s35, s34, 31
	s_lshl_b64 s[34:35], s[34:35], 12
	s_add_u32 s34, s44, s34
	v_ashrrev_i32_e32 v143, 31, v142
	s_addc_u32 s35, s16, s35
	v_lshl_add_u64 v[26:27], v[142:143], 2, s[34:35]
	v_ashrrev_i32_e32 v25, 31, v24
	v_lshl_add_u64 v[28:29], v[24:25], 2, s[14:15]
	v_mov_b32_e32 v28, v195
	v_lshlrev_b64 v[24:25], 11, v[24:25]
	v_lshl_add_u64 v[24:25], s[10:11], 0, v[24:25]
	v_pk_add_f32 v[14:15], v[14:15], v[166:167]
	v_pk_add_f32 v[10:11], v[10:11], v[170:171]
	v_pk_add_f32 v[8:9], v[8:9], v[168:169]
	v_pk_add_f32 v[12:13], v[12:13], v[164:165]
	v_lshl_add_u64 v[16:17], v[142:143], 1, v[24:25]
	v_pk_mul_f32 v[18:19], v[28:29], v[10:11] op_sel_hi:[0,1]
	v_pk_mul_f32 v[10:11], v[28:29], v[8:9] op_sel_hi:[0,1]
	v_pk_mul_f32 v[14:15], v[28:29], v[14:15] op_sel_hi:[0,1]
	v_pk_mul_f32 v[12:13], v[28:29], v[12:13] op_sel_hi:[0,1]
	v_cvt_pk_bf16_f32 v8, v12, v13
	v_cvt_pk_bf16_f32 v9, v14, v15
	v_cvt_pk_bf16_f32 v10, v10, v11
	v_cvt_pk_bf16_f32 v11, v18, v19
	global_store_dwordx4 v[16:17], v[8:11], off
	v_pk_add_f32 v[6:7], v[6:7], v[174:175]
	v_pk_add_f32 v[2:3], v[2:3], v[178:179]
	v_pk_add_f32 v[0:1], v[0:1], v[176:177]
	v_pk_add_f32 v[4:5], v[4:5], v[172:173]
	v_pk_mul_f32 v[8:9], v[28:29], v[2:3] op_sel_hi:[0,1]
	v_pk_mul_f32 v[2:3], v[28:29], v[0:1] op_sel_hi:[0,1]
	v_pk_mul_f32 v[6:7], v[28:29], v[6:7] op_sel_hi:[0,1]
	v_pk_mul_f32 v[4:5], v[28:29], v[4:5] op_sel_hi:[0,1]
	v_cvt_pk_bf16_f32 v0, v4, v5
	v_cvt_pk_bf16_f32 v1, v6, v7
	v_cvt_pk_bf16_f32 v2, v2, v3
	v_cvt_pk_bf16_f32 v3, v8, v9
	global_store_dwordx4 v[16:17], v[0:3], off offset:256
